# P6 epilogue stores also lane-permuted for contiguous 32-byte row pieces, store issued ~14 instructions behind its permutes (latency under the arithmetic); P7 as v79
# baseline (speedup 1.0000x reference)
.LBB0_781:
	s_ashr_i32 s37, s36, 31
	v_lshl_or_b32 v20, s34, 7, v210
	s_lshl_b64 s[36:37], s[36:37], 13
	s_add_u32 s38, s48, s36
	v_ashrrev_i32_e32 v21, 31, v20
	s_addc_u32 s39, s49, s37
	v_lshlrev_b64 v[2:3], 2, v[20:21]
	v_lshl_add_u64 v[8:9], s[38:39], 0, v[2:3]
	global_load_dwordx4 v[4:7], v[8:9], off
	global_load_dwordx4 v[12:15], v[8:9], off offset:16
	s_add_u32 s36, s52, s36
	s_addc_u32 s37, s53, s37
	v_lshl_add_u64 v[2:3], s[36:37], 0, v[2:3]
	global_load_dwordx4 v[24:27], v[2:3], off
	global_load_dwordx4 v[28:31], v[2:3], off offset:16
	v_mbcnt_lo_u32_b32 v18, -1, 0
	v_mbcnt_hi_u32_b32 v18, -1, v18
	v_lshrrev_b32_e32 v16, 2, v18
	v_and_b32_e32 v17, 15, v18
	v_sub_u32_e32 v16, v16, v17
	v_and_b32_e32 v17, 3, v18
	v_bfe_u32 v252, v18, 4, 2
	v_sub_u32_e32 v17, v17, v252
	v_lshlrev_b32_e32 v16, 11, v16
	v_lshl_add_u32 v16, v17, 3, v16
	v_ashrrev_i32_e32 v17, 31, v16
	v_and_b32_e32 v252, 3, v18
	v_lshlrev_b32_e32 v252, 4, v252
	v_lshrrev_b32_e32 v18, 2, v18
	v_add_lshl_u32 v252, v252, v18, 2
	v_lshl_add_u64 v[20:21], v[20:21], 0, v[16:17]
	v_lshl_add_u32 v22, s82, 8, v207
	v_ashrrev_i32_e32 v23, 31, v22
	v_lshlrev_b64 v[2:3], 11, v[22:23]
	v_mov_b32_e32 v32, v163
	v_mov_b32_e32 v33, v163
	v_lshl_add_u64 v[2:3], s[14:15], 0, v[2:3]
	v_lshl_add_u64 v[2:3], v[2:3], 0, v[20:21]
	s_mov_b64 s[98:99], s[0:1]
	s_andn2_b64 vcc, exec, s[0:1]
	s_cbranch_vccnz .Lp6u_done
	v_mov_b32_e32 v178, v170
	v_mov_b32_e32 v176, v162
	v_mov_b32_e32 v182, v174
	v_mov_b32_e32 v180, v172
	s_mov_b32 s36, s28
	s_mov_b32 s34, s26
	s_mov_b32 s82, s80
	s_mov_b64 s[40:41], s[30:31]
	s_add_i32 s66, s66, 1
	s_mul_i32 s0, s66, s67
	s_mul_hi_u32 s1, s66, s94
	s_add_i32 s1, s1, s0
	s_mul_i32 s0, s66, s94
	v_readlane_b32 s27, v254, 18
	s_add_u32 s38, s0, s27
	s_addc_u32 s39, s1, s54
	v_cmp_lt_i64_e64 s[0:1], s[38:39], v[168:169]
	s_mov_b64 s[30:31], -1
	s_and_b64 vcc, exec, s[0:1]
	s_cbranch_vccnz .Lp6u_774
	s_ashr_i32 s29, s28, 31
	s_mov_b64 s[30:31], 0

.LBB0_783:
	s_nop 15
	s_nop 15
	s_waitcnt vmcnt(0)
	v_pk_mul_f32 v[8:9], v[6:7], s[20:21] op_sel_hi:[1,0]
	v_pk_mul_f32 v[10:11], v[4:5], s[20:21] op_sel_hi:[1,0]
	v_pk_mul_f32 v[6:7], v[12:13], s[20:21] op_sel_hi:[1,0]
	v_pk_mul_f32 v[4:5], v[14:15], s[20:21] op_sel_hi:[1,0]
	v_pk_fma_f32 v[158:159], v[158:159], s[22:23], v[10:11] op_sel_hi:[1,0,1]
	v_pk_fma_f32 v[154:155], v[154:155], s[22:23], v[6:7] op_sel_hi:[1,0,1]
	v_pk_fma_f32 v[156:157], v[156:157], s[22:23], v[4:5] op_sel_hi:[1,0,1]
	v_pk_add_f32 v[16:17], v[26:27], 1.0 op_sel_hi:[1,0]
	v_pk_add_f32 v[18:19], v[24:25], 1.0 op_sel_hi:[1,0]
	v_min_f32_e32 v24, 0x42600000, v158
	v_min_f32_e32 v26, 0x42600000, v154
	v_min_f32_e32 v25, 0x42600000, v159
	v_min_f32_e32 v27, 0x42600000, v155
	v_pk_add_f32 v[12:13], v[30:31], 1.0 op_sel_hi:[1,0]
	v_min_f32_e32 v31, 0x42600000, v157
	v_mul_f32_e32 v23, 0xbe9d265f, v24
	v_mul_f32_e32 v155, 0xbe9d265f, v26
	v_mul_f32_e32 v157, 0xbe9d265f, v25
	v_mul_f32_e32 v158, 0xbe9d265f, v27
	v_min_f32_e32 v30, 0x42600000, v156
	v_exp_f32_e32 v154, v23
	v_exp_f32_e32 v156, v155
	v_exp_f32_e32 v155, v157
	v_exp_f32_e32 v157, v158
	v_pk_fma_f32 v[160:161], v[160:161], s[22:23], v[8:9] op_sel_hi:[1,0,1]
	v_pk_add_f32 v[14:15], v[28:29], 1.0 op_sel_hi:[1,0]
	v_min_f32_e32 v28, 0x42600000, v160
	v_min_f32_e32 v29, 0x42600000, v161
	v_pk_fma_f32 v[144:145], v[144:145], s[24:25], v[16:17] op_sel_hi:[1,0,1]
	v_pk_fma_f32 v[140:141], v[140:141], s[24:25], v[12:13] op_sel_hi:[1,0,1]
	v_mul_f32_e32 v159, 0xbe9d265f, v28
	v_mul_f32_e32 v160, 0xbe9d265f, v30
	v_mul_f32_e32 v161, 0xbe9d265f, v29
	v_mul_f32_e32 v171, 0xbe9d265f, v31
	v_med3_f32 v144, v144, s76, v213
	v_med3_f32 v140, v140, s76, v213
	v_med3_f32 v145, v145, s76, v213
	v_med3_f32 v141, v141, s76, v213
	v_exp_f32_e32 v158, v159
	v_exp_f32_e32 v160, v160
	v_exp_f32_e32 v159, v161
	v_exp_f32_e32 v161, v171
	v_pk_mul_f32 v[28:29], v[28:29], v[144:145]
	v_pk_mul_f32 v[30:31], v[30:31], v[140:141]
	v_pk_add_f32 v[140:141], v[154:155], 1.0 op_sel_hi:[1,0]
	v_pk_add_f32 v[144:145], v[156:157], 1.0 op_sel_hi:[1,0]
	v_rcp_f32_e32 v140, v140
	v_rcp_f32_e32 v144, v144
	v_rcp_f32_e32 v141, v141
	v_rcp_f32_e32 v145, v145
	v_pk_fma_f32 v[142:143], v[142:143], s[24:25], v[18:19] op_sel_hi:[1,0,1]
	v_pk_fma_f32 v[138:139], v[138:139], s[24:25], v[14:15] op_sel_hi:[1,0,1]
	v_med3_f32 v142, v142, s76, v213
	v_med3_f32 v138, v138, s76, v213
	v_med3_f32 v143, v143, s76, v213
	v_med3_f32 v139, v139, s76, v213
	v_pk_mul_f32 v[24:25], v[24:25], v[142:143]
	v_pk_mul_f32 v[26:27], v[26:27], v[138:139]
	v_pk_add_f32 v[138:139], v[158:159], 1.0 op_sel_hi:[1,0]
	v_pk_add_f32 v[142:143], v[160:161], 1.0 op_sel_hi:[1,0]
	v_rcp_f32_e32 v138, v138
	v_rcp_f32_e32 v142, v142
	v_rcp_f32_e32 v139, v139
	v_rcp_f32_e32 v143, v143
	v_pk_mul_f32 v[24:25], v[24:25], v[140:141]
	v_pk_mul_f32 v[26:27], v[26:27], v[144:145]
	v_cvt_pk_fp8_f32 v32, v24, v25
	v_cvt_pk_fp8_f32 v33, v26, v27
	v_pk_mul_f32 v[24:25], v[28:29], v[138:139]
	v_pk_mul_f32 v[26:27], v[30:31], v[142:143]
	v_cvt_pk_fp8_f32 v32, v24, v25 op_sel:[0,0,1]
	ds_bpermute_b32 v200, v252, v32
	v_cvt_pk_fp8_f32 v33, v26, v27 op_sel:[0,0,1]
	ds_bpermute_b32 v201, v252, v33
	v_pk_fma_f32 v[152:153], v[152:153], s[22:23], v[8:9] op_sel_hi:[1,0,1]
	v_pk_fma_f32 v[150:151], v[150:151], s[22:23], v[10:11] op_sel_hi:[1,0,1]
	v_pk_fma_f32 v[148:149], v[148:149], s[22:23], v[4:5] op_sel_hi:[1,0,1]
	v_pk_fma_f32 v[146:147], v[146:147], s[22:23], v[6:7] op_sel_hi:[1,0,1]
	v_min_f32_e32 v150, 0x42600000, v150
	v_pk_fma_f32 v[134:135], v[134:135], s[24:25], v[18:19] op_sel_hi:[1,0,1]
	v_min_f32_e32 v28, 0x42600000, v152
	v_min_f32_e32 v146, 0x42600000, v146
	v_pk_fma_f32 v[136:137], v[136:137], s[24:25], v[16:17] op_sel_hi:[1,0,1]
	v_pk_fma_f32 v[132:133], v[132:133], s[24:25], v[12:13] op_sel_hi:[1,0,1]
	v_med3_f32 v27, v135, s76, v213
	v_min_f32_e32 v30, 0x42600000, v148
	v_mul_f32_e32 v23, 0xbe9d265f, v150
	v_mul_f32_e32 v135, 0xbe9d265f, v28
	v_pk_fma_f32 v[24:25], v[130:131], s[24:25], v[14:15] op_sel_hi:[1,0,1]
	v_mov_b64_e32 v[202:203], v[2:3]
	v_min_f32_e32 v151, 0x42600000, v151
	v_med3_f32 v32, v136, s76, v213
	v_med3_f32 v130, v132, s76, v213
	v_min_f32_e32 v29, 0x42600000, v153
	v_exp_f32_e32 v132, v23
	v_mul_f32_e32 v23, 0xbe9d265f, v146
	v_exp_f32_e32 v136, v135
	v_mul_f32_e32 v135, 0xbe9d265f, v30
	v_med3_f32 v26, v134, s76, v213
	v_min_f32_e32 v147, 0x42600000, v147
	v_min_f32_e32 v31, 0x42600000, v149
	v_exp_f32_e32 v134, v23
	v_mul_f32_e32 v23, 0xbe9d265f, v151
	v_exp_f32_e32 v138, v135
	s_waitcnt lgkmcnt(0)
	global_store_dwordx2 v[202:203], v[200:201], off
	v_mul_f32_e32 v135, 0xbe9d265f, v29
	v_med3_f32 v33, v137, s76, v213
	v_med3_f32 v131, v133, s76, v213
	v_exp_f32_e32 v133, v23
	v_mul_f32_e32 v23, 0xbe9d265f, v147
	v_exp_f32_e32 v137, v135
	v_mul_f32_e32 v135, 0xbe9d265f, v31
	v_exp_f32_e32 v139, v135
	v_exp_f32_e32 v135, v23
	v_pk_add_f32 v[132:133], v[132:133], 1.0 op_sel_hi:[1,0]
	v_med3_f32 v24, v24, s76, v213
	v_rcp_f32_e32 v132, v132
	v_pk_add_f32 v[134:135], v[134:135], 1.0 op_sel_hi:[1,0]
	v_rcp_f32_e32 v133, v133
	v_rcp_f32_e32 v134, v134
	v_rcp_f32_e32 v135, v135
	v_med3_f32 v25, v25, s76, v213
	v_pk_add_f32 v[138:139], v[138:139], 1.0 op_sel_hi:[1,0]
	v_pk_mul_f32 v[24:25], v[146:147], v[24:25]
	v_pk_add_f32 v[136:137], v[136:137], 1.0 op_sel_hi:[1,0]
	v_rcp_f32_e32 v138, v138
	v_rcp_f32_e32 v139, v139
	v_pk_mul_f32 v[28:29], v[28:29], v[32:33]
	v_pk_mul_f32 v[26:27], v[150:151], v[26:27]
	v_pk_mul_f32 v[24:25], v[24:25], v[134:135]
	v_mov_b32_e32 v33, v163
	v_rcp_f32_e32 v136, v136
	v_rcp_f32_e32 v137, v137
	v_pk_mul_f32 v[26:27], v[26:27], v[132:133]
	v_mov_b32_e32 v32, v163
	v_cvt_pk_fp8_f32 v33, v24, v25
	v_cvt_pk_fp8_f32 v32, v26, v27
	v_pk_mul_f32 v[24:25], v[30:31], v[130:131]
	v_pk_mul_f32 v[28:29], v[28:29], v[136:137]
	v_pk_mul_f32 v[24:25], v[24:25], v[138:139]
	v_cvt_pk_fp8_f32 v32, v28, v29 op_sel:[0,0,1]
	ds_bpermute_b32 v200, v252, v32
	v_cvt_pk_fp8_f32 v33, v24, v25 op_sel:[0,0,1]
	ds_bpermute_b32 v201, v252, v33
	v_or_b32_e32 v24, 16, v22
	v_ashrrev_i32_e32 v25, 31, v24
	v_lshlrev_b64 v[24:25], 11, v[24:25]
	v_lshl_add_u64 v[24:25], s[14:15], 0, v[24:25]
	v_lshl_add_u64 v[24:25], v[24:25], 0, v[20:21]
	v_mov_b64_e32 v[202:203], v[24:25]
	v_pk_fma_f32 v[24:25], v[128:129], s[22:23], v[8:9] op_sel_hi:[1,0,1]
	v_pk_fma_f32 v[26:27], v[126:127], s[22:23], v[10:11] op_sel_hi:[1,0,1]
	v_pk_fma_f32 v[28:29], v[124:125], s[22:23], v[4:5] op_sel_hi:[1,0,1]
	v_pk_fma_f32 v[30:31], v[122:123], s[22:23], v[6:7] op_sel_hi:[1,0,1]
	v_min_f32_e32 v26, 0x42600000, v26
	v_min_f32_e32 v24, 0x42600000, v24
	v_min_f32_e32 v30, 0x42600000, v30
	v_min_f32_e32 v28, 0x42600000, v28
	v_mul_f32_e32 v23, 0xbe9d265f, v26
	v_mul_f32_e32 v123, 0xbe9d265f, v24
	v_pk_fma_f32 v[32:33], v[120:121], s[24:25], v[16:17] op_sel_hi:[1,0,1]
	v_min_f32_e32 v27, 0x42600000, v27
	v_min_f32_e32 v25, 0x42600000, v25
	v_exp_f32_e32 v120, v23
	s_waitcnt lgkmcnt(0)
	global_store_dwordx2 v[202:203], v[200:201], off
	v_mul_f32_e32 v23, 0xbe9d265f, v30
	v_exp_f32_e32 v124, v123
	v_mul_f32_e32 v123, 0xbe9d265f, v28
	v_min_f32_e32 v31, 0x42600000, v31
	v_min_f32_e32 v29, 0x42600000, v29
	v_exp_f32_e32 v122, v23
	v_mul_f32_e32 v23, 0xbe9d265f, v27
	v_exp_f32_e32 v126, v123
	v_mul_f32_e32 v123, 0xbe9d265f, v25
	v_exp_f32_e32 v121, v23
	v_mul_f32_e32 v23, 0xbe9d265f, v31
	v_exp_f32_e32 v125, v123
	v_mul_f32_e32 v123, 0xbe9d265f, v29
	v_exp_f32_e32 v127, v123
	v_exp_f32_e32 v123, v23
	v_pk_add_f32 v[120:121], v[120:121], 1.0 op_sel_hi:[1,0]
	v_pk_fma_f32 v[118:119], v[118:119], s[24:25], v[18:19] op_sel_hi:[1,0,1]
	v_rcp_f32_e32 v120, v120
	v_pk_add_f32 v[122:123], v[122:123], 1.0 op_sel_hi:[1,0]
	v_rcp_f32_e32 v121, v121
	v_rcp_f32_e32 v122, v122
	v_rcp_f32_e32 v123, v123
	v_pk_fma_f32 v[114:115], v[114:115], s[24:25], v[14:15] op_sel_hi:[1,0,1]
	v_med3_f32 v118, v118, s76, v213
	v_med3_f32 v119, v119, s76, v213
	v_med3_f32 v114, v114, s76, v213
	v_med3_f32 v115, v115, s76, v213
	v_med3_f32 v32, v32, s76, v213
	v_med3_f32 v33, v33, s76, v213
	v_pk_add_f32 v[124:125], v[124:125], 1.0 op_sel_hi:[1,0]
	v_pk_mul_f32 v[26:27], v[26:27], v[118:119]
	v_pk_add_f32 v[126:127], v[126:127], 1.0 op_sel_hi:[1,0]
	v_rcp_f32_e32 v124, v124
	v_rcp_f32_e32 v125, v125
	v_pk_mul_f32 v[24:25], v[24:25], v[32:33]
	v_pk_mul_f32 v[26:27], v[26:27], v[120:121]
	v_pk_mul_f32 v[30:31], v[30:31], v[114:115]
	v_mov_b32_e32 v32, v163
	v_rcp_f32_e32 v126, v126
	v_rcp_f32_e32 v127, v127
	v_pk_mul_f32 v[30:31], v[30:31], v[122:123]
	v_cvt_pk_fp8_f32 v32, v26, v27
	v_mov_b32_e32 v33, v163
	v_pk_fma_f32 v[116:117], v[116:117], s[24:25], v[12:13] op_sel_hi:[1,0,1]
	v_cvt_pk_fp8_f32 v33, v30, v31
	v_med3_f32 v116, v116, s76, v213
	v_med3_f32 v117, v117, s76, v213
	v_pk_mul_f32 v[24:25], v[24:25], v[124:125]
	v_pk_mul_f32 v[26:27], v[28:29], v[116:117]
	v_cvt_pk_fp8_f32 v32, v24, v25 op_sel:[0,0,1]
	ds_bpermute_b32 v200, v252, v32
	v_pk_mul_f32 v[26:27], v[26:27], v[126:127]
	v_or_b32_e32 v24, 32, v22
	v_cvt_pk_fp8_f32 v33, v26, v27 op_sel:[0,0,1]
	ds_bpermute_b32 v201, v252, v33
	v_ashrrev_i32_e32 v25, 31, v24
	v_lshlrev_b64 v[24:25], 11, v[24:25]
	v_lshl_add_u64 v[24:25], s[14:15], 0, v[24:25]
	v_lshl_add_u64 v[24:25], v[24:25], 0, v[20:21]
	v_mov_b64_e32 v[202:203], v[24:25]
	v_pk_fma_f32 v[24:25], v[112:113], s[22:23], v[8:9] op_sel_hi:[1,0,1]
	v_pk_fma_f32 v[26:27], v[110:111], s[22:23], v[10:11] op_sel_hi:[1,0,1]
	v_pk_fma_f32 v[28:29], v[108:109], s[22:23], v[4:5] op_sel_hi:[1,0,1]
	v_pk_fma_f32 v[30:31], v[106:107], s[22:23], v[6:7] op_sel_hi:[1,0,1]
	v_min_f32_e32 v26, 0x42600000, v26
	v_min_f32_e32 v24, 0x42600000, v24
	v_min_f32_e32 v30, 0x42600000, v30
	v_min_f32_e32 v28, 0x42600000, v28
	v_mul_f32_e32 v23, 0xbe9d265f, v26
	v_mul_f32_e32 v107, 0xbe9d265f, v24
	v_pk_fma_f32 v[32:33], v[104:105], s[24:25], v[16:17] op_sel_hi:[1,0,1]
	v_min_f32_e32 v27, 0x42600000, v27
	v_min_f32_e32 v25, 0x42600000, v25
	v_exp_f32_e32 v104, v23
	s_waitcnt lgkmcnt(0)
	global_store_dwordx2 v[202:203], v[200:201], off
	v_mul_f32_e32 v23, 0xbe9d265f, v30
	v_exp_f32_e32 v108, v107
	v_mul_f32_e32 v107, 0xbe9d265f, v28
	v_min_f32_e32 v31, 0x42600000, v31
	v_min_f32_e32 v29, 0x42600000, v29
	v_exp_f32_e32 v106, v23
	v_mul_f32_e32 v23, 0xbe9d265f, v27
	v_exp_f32_e32 v110, v107
	v_mul_f32_e32 v107, 0xbe9d265f, v25
	v_exp_f32_e32 v105, v23
	v_mul_f32_e32 v23, 0xbe9d265f, v31
	v_exp_f32_e32 v109, v107
	v_mul_f32_e32 v107, 0xbe9d265f, v29
	v_exp_f32_e32 v111, v107
	v_exp_f32_e32 v107, v23
	v_pk_add_f32 v[104:105], v[104:105], 1.0 op_sel_hi:[1,0]
	v_pk_fma_f32 v[102:103], v[102:103], s[24:25], v[18:19] op_sel_hi:[1,0,1]
	v_rcp_f32_e32 v104, v104
	v_pk_add_f32 v[106:107], v[106:107], 1.0 op_sel_hi:[1,0]
	v_rcp_f32_e32 v105, v105
	v_rcp_f32_e32 v106, v106
	v_rcp_f32_e32 v107, v107
	v_pk_fma_f32 v[98:99], v[98:99], s[24:25], v[14:15] op_sel_hi:[1,0,1]
	v_med3_f32 v102, v102, s76, v213
	v_med3_f32 v98, v98, s76, v213
	v_med3_f32 v103, v103, s76, v213
	v_med3_f32 v99, v99, s76, v213
	v_med3_f32 v32, v32, s76, v213
	v_med3_f32 v33, v33, s76, v213
	v_pk_add_f32 v[108:109], v[108:109], 1.0 op_sel_hi:[1,0]
	v_pk_add_f32 v[110:111], v[110:111], 1.0 op_sel_hi:[1,0]
	v_pk_mul_f32 v[26:27], v[26:27], v[102:103]
	v_pk_mul_f32 v[30:31], v[30:31], v[98:99]
	v_rcp_f32_e32 v108, v108
	v_rcp_f32_e32 v110, v110
	v_rcp_f32_e32 v109, v109
	v_rcp_f32_e32 v111, v111
	v_pk_mul_f32 v[24:25], v[24:25], v[32:33]
	v_pk_mul_f32 v[26:27], v[26:27], v[104:105]
	v_pk_mul_f32 v[30:31], v[30:31], v[106:107]
	v_mov_b32_e32 v32, v163
	v_mov_b32_e32 v33, v163
	v_pk_fma_f32 v[100:101], v[100:101], s[24:25], v[12:13] op_sel_hi:[1,0,1]
	v_cvt_pk_fp8_f32 v32, v26, v27
	v_cvt_pk_fp8_f32 v33, v30, v31
	v_med3_f32 v100, v100, s76, v213
	v_med3_f32 v101, v101, s76, v213
	v_pk_mul_f32 v[26:27], v[28:29], v[100:101]
	v_pk_mul_f32 v[24:25], v[24:25], v[108:109]
	v_pk_mul_f32 v[26:27], v[26:27], v[110:111]
	v_or_b32_e32 v22, 48, v22
	v_cvt_pk_fp8_f32 v32, v24, v25 op_sel:[0,0,1]
	ds_bpermute_b32 v200, v252, v32
	v_cvt_pk_fp8_f32 v33, v26, v27 op_sel:[0,0,1]
	ds_bpermute_b32 v201, v252, v33
	v_ashrrev_i32_e32 v23, 31, v22
	v_lshlrev_b64 v[22:23], 11, v[22:23]
	v_lshl_add_u64 v[22:23], s[14:15], 0, v[22:23]
	v_pk_fma_f32 v[26:27], v[90:91], s[22:23], v[6:7] op_sel_hi:[1,0,1]
	v_lshl_add_u64 v[20:21], v[22:23], 0, v[20:21]
	v_pk_fma_f32 v[22:23], v[94:95], s[22:23], v[10:11] op_sel_hi:[1,0,1]
	v_min_f32_e32 v26, 0x42600000, v26
	v_mov_b64_e32 v[202:203], v[20:21]
	v_pk_fma_f32 v[32:33], v[84:85], s[24:25], v[12:13] op_sel_hi:[1,0,1]
	v_min_f32_e32 v22, 0x42600000, v22
	v_min_f32_e32 v23, 0x42600000, v23
	v_min_f32_e32 v27, 0x42600000, v27
	v_mul_f32_e32 v85, 0xbe9d265f, v26
	v_pk_fma_f32 v[30:31], v[86:87], s[24:25], v[18:19] op_sel_hi:[1,0,1]
	v_mul_f32_e32 v84, 0xbe9d265f, v22
	v_exp_f32_e32 v86, v85
	v_mul_f32_e32 v85, 0xbe9d265f, v23
	v_mul_f32_e32 v87, 0xbe9d265f, v27
	v_pk_fma_f32 v[24:25], v[92:93], s[22:23], v[4:5] op_sel_hi:[1,0,1]
	v_exp_f32_e32 v84, v84
	v_exp_f32_e32 v85, v85
	v_exp_f32_e32 v87, v87
	s_waitcnt lgkmcnt(0)
	global_store_dwordx2 v[202:203], v[200:201], off
	v_pk_fma_f32 v[20:21], v[96:97], s[22:23], v[8:9] op_sel_hi:[1,0,1]
	v_min_f32_e32 v24, 0x42600000, v24
	v_pk_fma_f32 v[28:29], v[88:89], s[24:25], v[16:17] op_sel_hi:[1,0,1]
	v_min_f32_e32 v20, 0x42600000, v20
	v_min_f32_e32 v21, 0x42600000, v21
	v_min_f32_e32 v25, 0x42600000, v25
	v_mul_f32_e32 v89, 0xbe9d265f, v24
	v_mul_f32_e32 v88, 0xbe9d265f, v20
	v_exp_f32_e32 v90, v89
	v_mul_f32_e32 v89, 0xbe9d265f, v21
	v_mul_f32_e32 v91, 0xbe9d265f, v25
	v_exp_f32_e32 v88, v88
	v_exp_f32_e32 v89, v89
	v_exp_f32_e32 v91, v91
	v_pk_add_f32 v[84:85], v[84:85], 1.0 op_sel_hi:[1,0]
	v_pk_add_f32 v[86:87], v[86:87], 1.0 op_sel_hi:[1,0]
	v_rcp_f32_e32 v84, v84
	v_rcp_f32_e32 v86, v86
	v_rcp_f32_e32 v85, v85
	v_rcp_f32_e32 v87, v87
	v_pk_fma_f32 v[82:83], v[82:83], s[24:25], v[14:15] op_sel_hi:[1,0,1]
	v_med3_f32 v30, v30, s76, v213
	v_med3_f32 v82, v82, s76, v213
	v_med3_f32 v31, v31, s76, v213
	v_med3_f32 v83, v83, s76, v213
	v_med3_f32 v28, v28, s76, v213
	v_med3_f32 v29, v29, s76, v213
	v_pk_add_f32 v[88:89], v[88:89], 1.0 op_sel_hi:[1,0]
	v_pk_add_f32 v[90:91], v[90:91], 1.0 op_sel_hi:[1,0]
	v_pk_mul_f32 v[22:23], v[22:23], v[30:31]
	v_pk_mul_f32 v[26:27], v[26:27], v[82:83]
	v_rcp_f32_e32 v88, v88
	v_rcp_f32_e32 v90, v90
	v_rcp_f32_e32 v89, v89
	v_rcp_f32_e32 v91, v91
	v_pk_mul_f32 v[20:21], v[20:21], v[28:29]
	v_pk_mul_f32 v[22:23], v[22:23], v[84:85]
	v_pk_mul_f32 v[26:27], v[26:27], v[86:87]
	v_mov_b32_e32 v28, v163
	v_mov_b32_e32 v29, v163
	v_cvt_pk_fp8_f32 v28, v22, v23
	v_cvt_pk_fp8_f32 v29, v26, v27
	v_med3_f32 v32, v32, s76, v213
	v_med3_f32 v33, v33, s76, v213
	v_pk_mul_f32 v[22:23], v[24:25], v[32:33]
	v_pk_mul_f32 v[20:21], v[20:21], v[88:89]
	v_pk_mul_f32 v[22:23], v[22:23], v[90:91]
	v_pk_fma_f32 v[26:27], v[74:75], s[22:23], v[6:7] op_sel_hi:[1,0,1]
	v_cvt_pk_fp8_f32 v28, v20, v21 op_sel:[0,0,1]
	ds_bpermute_b32 v200, v252, v28
	v_cvt_pk_fp8_f32 v29, v22, v23 op_sel:[0,0,1]
	ds_bpermute_b32 v201, v252, v29
	v_pk_fma_f32 v[22:23], v[78:79], s[22:23], v[10:11] op_sel_hi:[1,0,1]
	v_min_f32_e32 v26, 0x42600000, v26
	v_pk_fma_f32 v[32:33], v[68:69], s[24:25], v[12:13] op_sel_hi:[1,0,1]
	v_min_f32_e32 v22, 0x42600000, v22
	v_min_f32_e32 v23, 0x42600000, v23
	v_min_f32_e32 v27, 0x42600000, v27
	v_mul_f32_e32 v69, 0xbe9d265f, v26
	v_add_co_u32_e32 v20, vcc, s77, v2
	v_pk_fma_f32 v[30:31], v[70:71], s[24:25], v[18:19] op_sel_hi:[1,0,1]
	v_mul_f32_e32 v68, 0xbe9d265f, v22
	v_exp_f32_e32 v70, v69
	v_mul_f32_e32 v69, 0xbe9d265f, v23
	v_mul_f32_e32 v71, 0xbe9d265f, v27
	v_addc_co_u32_e32 v21, vcc, 0, v3, vcc
	v_pk_fma_f32 v[24:25], v[76:77], s[22:23], v[4:5] op_sel_hi:[1,0,1]
	v_exp_f32_e32 v68, v68
	v_exp_f32_e32 v69, v69
	v_exp_f32_e32 v71, v71
	v_mov_b64_e32 v[202:203], v[20:21]
	v_pk_fma_f32 v[20:21], v[80:81], s[22:23], v[8:9] op_sel_hi:[1,0,1]
	v_min_f32_e32 v24, 0x42600000, v24
	v_pk_fma_f32 v[28:29], v[72:73], s[24:25], v[16:17] op_sel_hi:[1,0,1]
	v_min_f32_e32 v20, 0x42600000, v20
	v_min_f32_e32 v21, 0x42600000, v21
	v_min_f32_e32 v25, 0x42600000, v25
	v_mul_f32_e32 v73, 0xbe9d265f, v24
	v_mul_f32_e32 v72, 0xbe9d265f, v20
	v_exp_f32_e32 v74, v73
	v_mul_f32_e32 v73, 0xbe9d265f, v21
	v_mul_f32_e32 v75, 0xbe9d265f, v25
	v_exp_f32_e32 v72, v72
	v_exp_f32_e32 v73, v73
	v_exp_f32_e32 v75, v75
	s_waitcnt lgkmcnt(0)
	global_store_dwordx2 v[202:203], v[200:201], off
	v_pk_add_f32 v[68:69], v[68:69], 1.0 op_sel_hi:[1,0]
	v_pk_add_f32 v[70:71], v[70:71], 1.0 op_sel_hi:[1,0]
	v_rcp_f32_e32 v68, v68
	v_rcp_f32_e32 v70, v70
	v_rcp_f32_e32 v69, v69
	v_rcp_f32_e32 v71, v71
	v_pk_fma_f32 v[66:67], v[66:67], s[24:25], v[14:15] op_sel_hi:[1,0,1]
	v_med3_f32 v30, v30, s76, v213
	v_med3_f32 v66, v66, s76, v213
	v_med3_f32 v31, v31, s76, v213
	v_med3_f32 v67, v67, s76, v213
	v_med3_f32 v28, v28, s76, v213
	v_med3_f32 v29, v29, s76, v213
	v_pk_add_f32 v[72:73], v[72:73], 1.0 op_sel_hi:[1,0]
	v_pk_add_f32 v[74:75], v[74:75], 1.0 op_sel_hi:[1,0]
	v_pk_mul_f32 v[22:23], v[22:23], v[30:31]
	v_pk_mul_f32 v[26:27], v[26:27], v[66:67]
	v_rcp_f32_e32 v72, v72
	v_rcp_f32_e32 v74, v74
	v_rcp_f32_e32 v73, v73
	v_rcp_f32_e32 v75, v75
	v_pk_mul_f32 v[20:21], v[20:21], v[28:29]
	v_pk_mul_f32 v[22:23], v[22:23], v[68:69]
	v_pk_mul_f32 v[26:27], v[26:27], v[70:71]
	v_mov_b32_e32 v28, v163
	v_mov_b32_e32 v29, v163
	v_cvt_pk_fp8_f32 v28, v22, v23
	v_cvt_pk_fp8_f32 v29, v26, v27
	v_med3_f32 v32, v32, s76, v213
	v_med3_f32 v33, v33, s76, v213
	v_pk_mul_f32 v[22:23], v[24:25], v[32:33]
	v_pk_mul_f32 v[20:21], v[20:21], v[72:73]
	v_pk_mul_f32 v[22:23], v[22:23], v[74:75]
	v_pk_fma_f32 v[26:27], v[58:59], s[22:23], v[6:7] op_sel_hi:[1,0,1]
	v_cvt_pk_fp8_f32 v28, v20, v21 op_sel:[0,0,1]
	ds_bpermute_b32 v200, v252, v28
	v_cvt_pk_fp8_f32 v29, v22, v23 op_sel:[0,0,1]
	ds_bpermute_b32 v201, v252, v29
	v_pk_fma_f32 v[22:23], v[62:63], s[22:23], v[10:11] op_sel_hi:[1,0,1]
	v_min_f32_e32 v26, 0x42600000, v26
	v_pk_fma_f32 v[32:33], v[52:53], s[24:25], v[12:13] op_sel_hi:[1,0,1]
	v_min_f32_e32 v22, 0x42600000, v22
	v_min_f32_e32 v23, 0x42600000, v23
	v_min_f32_e32 v27, 0x42600000, v27
	v_mul_f32_e32 v53, 0xbe9d265f, v26
	v_add_co_u32_e32 v20, vcc, s78, v2
	v_pk_fma_f32 v[30:31], v[54:55], s[24:25], v[18:19] op_sel_hi:[1,0,1]
	v_mul_f32_e32 v52, 0xbe9d265f, v22
	v_exp_f32_e32 v54, v53
	v_mul_f32_e32 v53, 0xbe9d265f, v23
	v_mul_f32_e32 v55, 0xbe9d265f, v27
	v_addc_co_u32_e32 v21, vcc, 0, v3, vcc
	v_pk_fma_f32 v[24:25], v[60:61], s[22:23], v[4:5] op_sel_hi:[1,0,1]
	v_exp_f32_e32 v52, v52
	v_exp_f32_e32 v53, v53
	v_exp_f32_e32 v55, v55
	v_mov_b64_e32 v[202:203], v[20:21]
	v_pk_fma_f32 v[20:21], v[64:65], s[22:23], v[8:9] op_sel_hi:[1,0,1]
	v_min_f32_e32 v24, 0x42600000, v24
	v_pk_fma_f32 v[28:29], v[56:57], s[24:25], v[16:17] op_sel_hi:[1,0,1]
	v_min_f32_e32 v20, 0x42600000, v20
	v_min_f32_e32 v21, 0x42600000, v21
	v_min_f32_e32 v25, 0x42600000, v25
	v_mul_f32_e32 v57, 0xbe9d265f, v24
	v_mul_f32_e32 v56, 0xbe9d265f, v20
	v_exp_f32_e32 v58, v57
	v_mul_f32_e32 v57, 0xbe9d265f, v21
	v_mul_f32_e32 v59, 0xbe9d265f, v25
	v_exp_f32_e32 v56, v56
	v_exp_f32_e32 v57, v57
	v_exp_f32_e32 v59, v59
	s_waitcnt lgkmcnt(0)
	global_store_dwordx2 v[202:203], v[200:201], off
	v_pk_add_f32 v[52:53], v[52:53], 1.0 op_sel_hi:[1,0]
	v_pk_add_f32 v[54:55], v[54:55], 1.0 op_sel_hi:[1,0]
	v_rcp_f32_e32 v52, v52
	v_rcp_f32_e32 v54, v54
	v_rcp_f32_e32 v53, v53
	v_rcp_f32_e32 v55, v55
	v_pk_fma_f32 v[50:51], v[50:51], s[24:25], v[14:15] op_sel_hi:[1,0,1]
	v_med3_f32 v30, v30, s76, v213
	v_med3_f32 v50, v50, s76, v213
	v_med3_f32 v31, v31, s76, v213
	v_med3_f32 v51, v51, s76, v213
	v_med3_f32 v28, v28, s76, v213
	v_med3_f32 v29, v29, s76, v213
	v_pk_add_f32 v[56:57], v[56:57], 1.0 op_sel_hi:[1,0]
	v_pk_add_f32 v[58:59], v[58:59], 1.0 op_sel_hi:[1,0]
	v_pk_mul_f32 v[22:23], v[22:23], v[30:31]
	v_pk_mul_f32 v[26:27], v[26:27], v[50:51]
	v_rcp_f32_e32 v56, v56
	v_rcp_f32_e32 v58, v58
	v_rcp_f32_e32 v57, v57
	v_rcp_f32_e32 v59, v59
	v_pk_mul_f32 v[20:21], v[20:21], v[28:29]
	v_pk_mul_f32 v[22:23], v[22:23], v[52:53]
	v_pk_mul_f32 v[26:27], v[26:27], v[54:55]
	v_mov_b32_e32 v28, v163
	v_mov_b32_e32 v29, v163
	v_cvt_pk_fp8_f32 v28, v22, v23
	v_cvt_pk_fp8_f32 v29, v26, v27
	v_med3_f32 v32, v32, s76, v213
	v_med3_f32 v33, v33, s76, v213
	v_pk_mul_f32 v[22:23], v[24:25], v[32:33]
	v_pk_mul_f32 v[20:21], v[20:21], v[56:57]
	v_pk_mul_f32 v[22:23], v[22:23], v[58:59]
	v_cvt_pk_fp8_f32 v28, v20, v21 op_sel:[0,0,1]
	ds_bpermute_b32 v200, v252, v28
	v_cvt_pk_fp8_f32 v29, v22, v23 op_sel:[0,0,1]
	ds_bpermute_b32 v201, v252, v29
	v_add_co_u32_e32 v20, vcc, s79, v2
	v_pk_fma_f32 v[6:7], v[42:43], s[22:23], v[6:7] op_sel_hi:[1,0,1]
	s_nop 0
	v_addc_co_u32_e32 v21, vcc, 0, v3, vcc
	v_pk_fma_f32 v[10:11], v[46:47], s[22:23], v[10:11] op_sel_hi:[1,0,1]
	v_min_f32_e32 v6, 0x42600000, v6
	v_mov_b64_e32 v[202:203], v[20:21]
	v_min_f32_e32 v10, 0x42600000, v10
	v_min_f32_e32 v11, 0x42600000, v11
	v_min_f32_e32 v7, 0x42600000, v7
	v_mul_f32_e32 v21, 0xbe9d265f, v6
	v_mul_f32_e32 v20, 0xbe9d265f, v10
	v_exp_f32_e32 v22, v21
	v_mul_f32_e32 v21, 0xbe9d265f, v11
	v_mul_f32_e32 v23, 0xbe9d265f, v7
	v_pk_fma_f32 v[4:5], v[44:45], s[22:23], v[4:5] op_sel_hi:[1,0,1]
	v_exp_f32_e32 v20, v20
	v_exp_f32_e32 v21, v21
	v_exp_f32_e32 v23, v23
	v_pk_fma_f32 v[8:9], v[48:49], s[22:23], v[8:9] op_sel_hi:[1,0,1]
	v_min_f32_e32 v4, 0x42600000, v4
	s_waitcnt lgkmcnt(0)
	global_store_dwordx2 v[202:203], v[200:201], off
	v_min_f32_e32 v8, 0x42600000, v8
	v_min_f32_e32 v9, 0x42600000, v9
	v_min_f32_e32 v5, 0x42600000, v5
	v_mul_f32_e32 v25, 0xbe9d265f, v4
	v_mul_f32_e32 v24, 0xbe9d265f, v8
	v_exp_f32_e32 v26, v25
	v_mul_f32_e32 v25, 0xbe9d265f, v9
	v_mul_f32_e32 v27, 0xbe9d265f, v5
	v_exp_f32_e32 v24, v24
	v_exp_f32_e32 v25, v25
	v_exp_f32_e32 v27, v27
	v_pk_add_f32 v[20:21], v[20:21], 1.0 op_sel_hi:[1,0]
	v_pk_add_f32 v[22:23], v[22:23], 1.0 op_sel_hi:[1,0]
	v_rcp_f32_e32 v20, v20
	v_rcp_f32_e32 v22, v22
	v_rcp_f32_e32 v21, v21
	v_rcp_f32_e32 v23, v23
	v_pk_fma_f32 v[18:19], v[38:39], s[24:25], v[18:19] op_sel_hi:[1,0,1]
	v_pk_fma_f32 v[14:15], v[34:35], s[24:25], v[14:15] op_sel_hi:[1,0,1]
	v_med3_f32 v18, v18, s76, v213
	v_med3_f32 v14, v14, s76, v213
	v_med3_f32 v19, v19, s76, v213
	v_med3_f32 v15, v15, s76, v213
	v_pk_add_f32 v[24:25], v[24:25], 1.0 op_sel_hi:[1,0]
	v_pk_add_f32 v[26:27], v[26:27], 1.0 op_sel_hi:[1,0]
	v_pk_mul_f32 v[10:11], v[10:11], v[18:19]
	v_pk_mul_f32 v[6:7], v[6:7], v[14:15]
	v_rcp_f32_e32 v24, v24
	v_rcp_f32_e32 v26, v26
	v_rcp_f32_e32 v25, v25
	v_rcp_f32_e32 v27, v27
	v_pk_mul_f32 v[10:11], v[10:11], v[20:21]
	v_pk_mul_f32 v[6:7], v[6:7], v[22:23]
	v_mov_b32_e32 v14, v163
	v_mov_b32_e32 v15, v163
	v_pk_fma_f32 v[16:17], v[40:41], s[24:25], v[16:17] op_sel_hi:[1,0,1]
	v_pk_fma_f32 v[12:13], v[36:37], s[24:25], v[12:13] op_sel_hi:[1,0,1]
	v_cvt_pk_fp8_f32 v14, v10, v11
	v_cvt_pk_fp8_f32 v15, v6, v7
	v_med3_f32 v16, v16, s76, v213
	v_med3_f32 v12, v12, s76, v213
	v_med3_f32 v17, v17, s76, v213
	v_med3_f32 v13, v13, s76, v213
	v_pk_mul_f32 v[8:9], v[8:9], v[16:17]
	v_pk_mul_f32 v[4:5], v[4:5], v[12:13]
	v_pk_mul_f32 v[8:9], v[8:9], v[24:25]
	v_pk_mul_f32 v[4:5], v[4:5], v[26:27]
	v_cvt_pk_fp8_f32 v14, v8, v9 op_sel:[0,0,1]
	ds_bpermute_b32 v200, v252, v14
	v_cvt_pk_fp8_f32 v15, v4, v5 op_sel:[0,0,1]
	ds_bpermute_b32 v201, v252, v15
	v_add_co_u32_e32 v2, vcc, 0x58000, v2
	s_nop 1
	v_addc_co_u32_e32 v3, vcc, 0, v3, vcc
	s_andn2_b64 vcc, exec, s[98:99]
	s_waitcnt lgkmcnt(0)
	global_store_dwordx2 v[2:3], v[200:201], off
	s_cbranch_vccnz .LBB0_786
	s_branch .Lp6_entry_pre
